# v049 + swiglu epilogues (P7, P16): seven of the eight per-store 64-bit row-address computations replaced by one pointer step each
# baseline (speedup 1.0000x reference)
.LBB0_786:
	s_lshl_b32 s88, s75, 4
	s_mov_b32 s89, 0
	s_mul_i32 s90, s75, 0x50
	s_mov_b32 s91, 0
	v_pk_mul_f32 v[156:157], v[126:127], s[44:45] op_sel_hi:[1,0]
	v_pk_mul_f32 v[122:123], v[126:127], v[122:123]
	v_exp_f32_e32 v156, v156
	v_exp_f32_e32 v157, v157
	v_pk_mul_f32 v[126:127], v[118:119], s[44:45] op_sel_hi:[1,0]
	v_pk_mul_f32 v[158:159], v[128:129], s[44:45] op_sel_hi:[1,0]
	v_exp_f32_e32 v126, v126
	v_exp_f32_e32 v127, v127
	v_pk_fma_f32 v[156:157], v[156:157], s[50:51], s[50:51] op_sel_hi:[1,0,0]
	v_pk_mul_f32 v[124:125], v[128:129], v[124:125]
	v_pk_mul_f32 v[128:129], v[120:121], s[44:45] op_sel_hi:[1,0]
	v_exp_f32_e32 v158, v158
	v_exp_f32_e32 v159, v159
	v_rcp_f32_e32 v156, v156
	v_rcp_f32_e32 v157, v157
	v_exp_f32_e32 v128, v128
	v_exp_f32_e32 v129, v129
	v_pk_fma_f32 v[126:127], v[126:127], s[50:51], s[50:51] op_sel_hi:[1,0,0]
	v_pk_fma_f32 v[158:159], v[158:159], s[50:51], s[50:51] op_sel_hi:[1,0,0]
	v_rcp_f32_e32 v126, v126
	v_rcp_f32_e32 v127, v127
	v_pk_mul_f32 v[122:123], v[156:157], v[122:123]
	v_pk_fma_f32 v[128:129], v[128:129], s[50:51], s[50:51] op_sel_hi:[1,0,0]
	v_pk_mul_f32 v[114:115], v[118:119], v[114:115]
	v_rcp_f32_e32 v158, v158
	v_rcp_f32_e32 v159, v159
	v_rcp_f32_e32 v128, v128
	v_rcp_f32_e32 v129, v129
	v_pk_mul_f32 v[116:117], v[120:121], v[116:117]
	v_pk_mul_f32 v[114:115], v[126:127], v[114:115]
	v_med3_f32 v119, v122, s80, v154
	v_med3_f32 v120, v123, s80, v154
	v_cvt_pk_fp8_f32 v118, v119, v120
	v_med3_f32 v114, v114, s80, v154
	v_med3_f32 v115, v115, s80, v154
	v_cvt_pk_fp8_f32 v119, v114, v115
	v_pk_mul_f32 v[124:125], v[158:159], v[124:125]
	v_pk_mul_f32 v[116:117], v[128:129], v[116:117]
	v_med3_f32 v120, v124, s80, v154
	v_med3_f32 v121, v125, s80, v154
	v_med3_f32 v114, v116, s80, v154
	v_med3_f32 v115, v117, s80, v154
	v_cvt_pk_fp8_f32 v118, v120, v121 op_sel:[0,0,1]
	v_cvt_pk_fp8_f32 v119, v114, v115 op_sel:[0,0,1]
	v_lshl_add_u32 v155, s60, 8, v148
	v_lshl_or_b32 v144, s2, 7, v150
	v_mov_b64_e32 v[146:147], s[14:15]
	v_ashrrev_i32_e32 v145, 31, v144
	v_mad_i64_i32 v[114:115], s[26:27], v155, s75, v[146:147]
	v_lshl_add_u64 v[114:115], v[114:115], 0, v[144:145]
	global_store_dwordx2 v[114:115], v[118:119], off
	v_lshl_add_u64 v[250:251], v[114:115], 0, s[88:89]
	v_pk_mul_f32 v[114:115], v[110:111], s[44:45] op_sel_hi:[1,0]
	v_pk_mul_f32 v[106:107], v[110:111], v[106:107]
	v_exp_f32_e32 v114, v114
	v_exp_f32_e32 v115, v115
	v_pk_mul_f32 v[110:111], v[102:103], s[44:45] op_sel_hi:[1,0]
	v_pk_mul_f32 v[116:117], v[112:113], s[44:45] op_sel_hi:[1,0]
	v_exp_f32_e32 v110, v110
	v_exp_f32_e32 v111, v111
	v_pk_fma_f32 v[114:115], v[114:115], s[50:51], s[50:51] op_sel_hi:[1,0,0]
	v_pk_mul_f32 v[108:109], v[112:113], v[108:109]
	v_pk_mul_f32 v[112:113], v[104:105], s[44:45] op_sel_hi:[1,0]
	v_exp_f32_e32 v116, v116
	v_exp_f32_e32 v117, v117
	v_rcp_f32_e32 v114, v114
	v_rcp_f32_e32 v115, v115
	v_exp_f32_e32 v112, v112
	v_exp_f32_e32 v113, v113
	v_pk_fma_f32 v[110:111], v[110:111], s[50:51], s[50:51] op_sel_hi:[1,0,0]
	v_pk_fma_f32 v[116:117], v[116:117], s[50:51], s[50:51] op_sel_hi:[1,0,0]
	v_rcp_f32_e32 v110, v110
	v_rcp_f32_e32 v111, v111
	v_pk_mul_f32 v[106:107], v[114:115], v[106:107]
	v_pk_fma_f32 v[112:113], v[112:113], s[50:51], s[50:51] op_sel_hi:[1,0,0]
	v_pk_mul_f32 v[98:99], v[102:103], v[98:99]
	v_rcp_f32_e32 v116, v116
	v_rcp_f32_e32 v117, v117
	v_rcp_f32_e32 v112, v112
	v_rcp_f32_e32 v113, v113
	v_pk_mul_f32 v[100:101], v[104:105], v[100:101]
	v_pk_mul_f32 v[98:99], v[110:111], v[98:99]
	v_med3_f32 v103, v106, s80, v154
	v_med3_f32 v104, v107, s80, v154
	v_cvt_pk_fp8_f32 v102, v103, v104
	v_med3_f32 v98, v98, s80, v154
	v_med3_f32 v99, v99, s80, v154
	v_cvt_pk_fp8_f32 v103, v98, v99
	v_pk_mul_f32 v[108:109], v[116:117], v[108:109]
	v_pk_mul_f32 v[100:101], v[112:113], v[100:101]
	v_med3_f32 v104, v108, s80, v154
	v_med3_f32 v105, v109, s80, v154
	v_med3_f32 v98, v100, s80, v154
	v_med3_f32 v99, v101, s80, v154
	v_cvt_pk_fp8_f32 v102, v104, v105 op_sel:[0,0,1]
	v_cvt_pk_fp8_f32 v103, v98, v99 op_sel:[0,0,1]
	global_store_dwordx2 v[250:251], v[102:103], off
	v_pk_mul_f32 v[98:99], v[94:95], s[44:45] op_sel_hi:[1,0]
	v_pk_mul_f32 v[90:91], v[94:95], v[90:91]
	v_exp_f32_e32 v98, v98
	v_exp_f32_e32 v99, v99
	v_pk_mul_f32 v[94:95], v[86:87], s[44:45] op_sel_hi:[1,0]
	v_pk_mul_f32 v[100:101], v[96:97], s[44:45] op_sel_hi:[1,0]
	v_exp_f32_e32 v94, v94
	v_exp_f32_e32 v95, v95
	v_pk_fma_f32 v[98:99], v[98:99], s[50:51], s[50:51] op_sel_hi:[1,0,0]
	v_pk_mul_f32 v[92:93], v[96:97], v[92:93]
	v_pk_mul_f32 v[96:97], v[88:89], s[44:45] op_sel_hi:[1,0]
	v_exp_f32_e32 v100, v100
	v_exp_f32_e32 v101, v101
	v_rcp_f32_e32 v98, v98
	v_rcp_f32_e32 v99, v99
	v_exp_f32_e32 v96, v96
	v_exp_f32_e32 v97, v97
	v_pk_fma_f32 v[94:95], v[94:95], s[50:51], s[50:51] op_sel_hi:[1,0,0]
	v_pk_fma_f32 v[100:101], v[100:101], s[50:51], s[50:51] op_sel_hi:[1,0,0]
	v_rcp_f32_e32 v94, v94
	v_rcp_f32_e32 v95, v95
	v_pk_mul_f32 v[90:91], v[98:99], v[90:91]
	v_pk_fma_f32 v[96:97], v[96:97], s[50:51], s[50:51] op_sel_hi:[1,0,0]
	v_pk_mul_f32 v[82:83], v[86:87], v[82:83]
	v_rcp_f32_e32 v100, v100
	v_rcp_f32_e32 v101, v101
	v_rcp_f32_e32 v96, v96
	v_rcp_f32_e32 v97, v97
	v_pk_mul_f32 v[84:85], v[88:89], v[84:85]
	v_pk_mul_f32 v[82:83], v[94:95], v[82:83]
	v_med3_f32 v87, v90, s80, v154
	v_med3_f32 v88, v91, s80, v154
	v_cvt_pk_fp8_f32 v86, v87, v88
	v_med3_f32 v82, v82, s80, v154
	v_med3_f32 v83, v83, s80, v154
	v_cvt_pk_fp8_f32 v87, v82, v83
	v_pk_mul_f32 v[92:93], v[100:101], v[92:93]
	v_pk_mul_f32 v[84:85], v[96:97], v[84:85]
	v_med3_f32 v88, v92, s80, v154
	v_med3_f32 v89, v93, s80, v154
	v_med3_f32 v82, v84, s80, v154
	v_med3_f32 v83, v85, s80, v154
	v_cvt_pk_fp8_f32 v86, v88, v89 op_sel:[0,0,1]
	v_cvt_pk_fp8_f32 v87, v82, v83 op_sel:[0,0,1]
	v_lshl_add_u64 v[250:251], v[250:251], 0, s[88:89]
	global_store_dwordx2 v[250:251], v[86:87], off
	v_pk_mul_f32 v[82:83], v[78:79], s[44:45] op_sel_hi:[1,0]
	v_pk_mul_f32 v[74:75], v[78:79], v[74:75]
	v_exp_f32_e32 v82, v82
	v_exp_f32_e32 v83, v83
	v_pk_mul_f32 v[78:79], v[70:71], s[44:45] op_sel_hi:[1,0]
	v_pk_mul_f32 v[84:85], v[80:81], s[44:45] op_sel_hi:[1,0]
	v_exp_f32_e32 v78, v78
	v_exp_f32_e32 v79, v79
	v_pk_fma_f32 v[82:83], v[82:83], s[50:51], s[50:51] op_sel_hi:[1,0,0]
	v_pk_mul_f32 v[76:77], v[80:81], v[76:77]
	v_pk_mul_f32 v[80:81], v[72:73], s[44:45] op_sel_hi:[1,0]
	v_exp_f32_e32 v84, v84
	v_exp_f32_e32 v85, v85
	v_rcp_f32_e32 v82, v82
	v_rcp_f32_e32 v83, v83
	v_exp_f32_e32 v80, v80
	v_exp_f32_e32 v81, v81
	v_pk_fma_f32 v[78:79], v[78:79], s[50:51], s[50:51] op_sel_hi:[1,0,0]
	v_pk_fma_f32 v[84:85], v[84:85], s[50:51], s[50:51] op_sel_hi:[1,0,0]
	v_rcp_f32_e32 v78, v78
	v_rcp_f32_e32 v79, v79
	v_pk_mul_f32 v[74:75], v[82:83], v[74:75]
	v_pk_fma_f32 v[80:81], v[80:81], s[50:51], s[50:51] op_sel_hi:[1,0,0]
	v_pk_mul_f32 v[66:67], v[70:71], v[66:67]
	v_rcp_f32_e32 v84, v84
	v_rcp_f32_e32 v85, v85
	v_rcp_f32_e32 v80, v80
	v_rcp_f32_e32 v81, v81
	v_pk_mul_f32 v[68:69], v[72:73], v[68:69]
	v_pk_mul_f32 v[66:67], v[78:79], v[66:67]
	v_med3_f32 v71, v74, s80, v154
	v_med3_f32 v72, v75, s80, v154
	v_cvt_pk_fp8_f32 v70, v71, v72
	v_med3_f32 v66, v66, s80, v154
	v_med3_f32 v67, v67, s80, v154
	v_cvt_pk_fp8_f32 v71, v66, v67
	v_pk_mul_f32 v[76:77], v[84:85], v[76:77]
	v_pk_mul_f32 v[68:69], v[80:81], v[68:69]
	v_med3_f32 v72, v76, s80, v154
	v_med3_f32 v73, v77, s80, v154
	v_med3_f32 v66, v68, s80, v154
	v_med3_f32 v67, v69, s80, v154
	v_cvt_pk_fp8_f32 v70, v72, v73 op_sel:[0,0,1]
	v_cvt_pk_fp8_f32 v71, v66, v67 op_sel:[0,0,1]
	v_lshl_add_u64 v[250:251], v[250:251], 0, s[88:89]
	global_store_dwordx2 v[250:251], v[70:71], off
	v_pk_mul_f32 v[66:67], v[62:63], s[44:45] op_sel_hi:[1,0]
	v_pk_mul_f32 v[58:59], v[62:63], v[58:59]
	v_exp_f32_e32 v66, v66
	v_exp_f32_e32 v67, v67
	v_pk_mul_f32 v[62:63], v[54:55], s[44:45] op_sel_hi:[1,0]
	v_pk_mul_f32 v[68:69], v[64:65], s[44:45] op_sel_hi:[1,0]
	v_exp_f32_e32 v62, v62
	v_exp_f32_e32 v63, v63
	v_pk_fma_f32 v[66:67], v[66:67], s[50:51], s[50:51] op_sel_hi:[1,0,0]
	v_pk_mul_f32 v[60:61], v[64:65], v[60:61]
	v_pk_mul_f32 v[64:65], v[56:57], s[44:45] op_sel_hi:[1,0]
	v_exp_f32_e32 v68, v68
	v_exp_f32_e32 v69, v69
	v_rcp_f32_e32 v66, v66
	v_rcp_f32_e32 v67, v67
	v_exp_f32_e32 v64, v64
	v_exp_f32_e32 v65, v65
	v_pk_fma_f32 v[62:63], v[62:63], s[50:51], s[50:51] op_sel_hi:[1,0,0]
	v_pk_fma_f32 v[68:69], v[68:69], s[50:51], s[50:51] op_sel_hi:[1,0,0]
	v_rcp_f32_e32 v62, v62
	v_rcp_f32_e32 v63, v63
	v_pk_mul_f32 v[58:59], v[66:67], v[58:59]
	v_pk_fma_f32 v[64:65], v[64:65], s[50:51], s[50:51] op_sel_hi:[1,0,0]
	v_pk_mul_f32 v[50:51], v[54:55], v[50:51]
	v_rcp_f32_e32 v68, v68
	v_rcp_f32_e32 v69, v69
	v_rcp_f32_e32 v64, v64
	v_rcp_f32_e32 v65, v65
	v_pk_mul_f32 v[52:53], v[56:57], v[52:53]
	v_pk_mul_f32 v[50:51], v[62:63], v[50:51]
	v_med3_f32 v55, v58, s80, v154
	v_med3_f32 v56, v59, s80, v154
	v_cvt_pk_fp8_f32 v54, v55, v56
	v_med3_f32 v50, v50, s80, v154
	v_med3_f32 v51, v51, s80, v154
	v_cvt_pk_fp8_f32 v55, v50, v51
	v_pk_mul_f32 v[60:61], v[68:69], v[60:61]
	v_pk_mul_f32 v[52:53], v[64:65], v[52:53]
	v_med3_f32 v56, v60, s80, v154
	v_med3_f32 v57, v61, s80, v154
	v_med3_f32 v50, v52, s80, v154
	v_med3_f32 v51, v53, s80, v154
	v_cvt_pk_fp8_f32 v54, v56, v57 op_sel:[0,0,1]
	v_cvt_pk_fp8_f32 v55, v50, v51 op_sel:[0,0,1]
	v_lshl_add_u64 v[250:251], v[250:251], 0, s[90:91]
	global_store_dwordx2 v[250:251], v[54:55], off
	v_pk_mul_f32 v[50:51], v[46:47], s[44:45] op_sel_hi:[1,0]
	v_pk_mul_f32 v[42:43], v[46:47], v[42:43]
	v_exp_f32_e32 v50, v50
	v_exp_f32_e32 v51, v51
	v_pk_mul_f32 v[46:47], v[38:39], s[44:45] op_sel_hi:[1,0]
	v_pk_mul_f32 v[52:53], v[48:49], s[44:45] op_sel_hi:[1,0]
	v_exp_f32_e32 v46, v46
	v_exp_f32_e32 v47, v47
	v_pk_fma_f32 v[50:51], v[50:51], s[50:51], s[50:51] op_sel_hi:[1,0,0]
	v_pk_mul_f32 v[44:45], v[48:49], v[44:45]
	v_pk_mul_f32 v[48:49], v[40:41], s[44:45] op_sel_hi:[1,0]
	v_exp_f32_e32 v52, v52
	v_exp_f32_e32 v53, v53
	v_rcp_f32_e32 v50, v50
	v_rcp_f32_e32 v51, v51
	v_exp_f32_e32 v48, v48
	v_exp_f32_e32 v49, v49
	v_pk_fma_f32 v[46:47], v[46:47], s[50:51], s[50:51] op_sel_hi:[1,0,0]
	v_pk_fma_f32 v[52:53], v[52:53], s[50:51], s[50:51] op_sel_hi:[1,0,0]
	v_rcp_f32_e32 v46, v46
	v_rcp_f32_e32 v47, v47
	v_pk_mul_f32 v[42:43], v[50:51], v[42:43]
	v_pk_fma_f32 v[48:49], v[48:49], s[50:51], s[50:51] op_sel_hi:[1,0,0]
	v_pk_mul_f32 v[34:35], v[38:39], v[34:35]
	v_rcp_f32_e32 v52, v52
	v_rcp_f32_e32 v53, v53
	v_rcp_f32_e32 v48, v48
	v_rcp_f32_e32 v49, v49
	v_pk_mul_f32 v[36:37], v[40:41], v[36:37]
	v_pk_mul_f32 v[34:35], v[46:47], v[34:35]
	v_med3_f32 v39, v42, s80, v154
	v_med3_f32 v40, v43, s80, v154
	v_cvt_pk_fp8_f32 v38, v39, v40
	v_med3_f32 v34, v34, s80, v154
	v_med3_f32 v35, v35, s80, v154
	v_cvt_pk_fp8_f32 v39, v34, v35
	v_pk_mul_f32 v[44:45], v[52:53], v[44:45]
	v_pk_mul_f32 v[36:37], v[48:49], v[36:37]
	v_med3_f32 v40, v44, s80, v154
	v_med3_f32 v41, v45, s80, v154
	v_med3_f32 v34, v36, s80, v154
	v_med3_f32 v35, v37, s80, v154
	v_cvt_pk_fp8_f32 v38, v40, v41 op_sel:[0,0,1]
	v_cvt_pk_fp8_f32 v39, v34, v35 op_sel:[0,0,1]
	v_lshl_add_u64 v[250:251], v[250:251], 0, s[88:89]
	global_store_dwordx2 v[250:251], v[38:39], off
	v_pk_mul_f32 v[34:35], v[30:31], s[44:45] op_sel_hi:[1,0]
	v_pk_mul_f32 v[26:27], v[30:31], v[26:27]
	v_exp_f32_e32 v34, v34
	v_exp_f32_e32 v35, v35
	v_pk_mul_f32 v[30:31], v[22:23], s[44:45] op_sel_hi:[1,0]
	v_pk_mul_f32 v[36:37], v[32:33], s[44:45] op_sel_hi:[1,0]
	v_exp_f32_e32 v30, v30
	v_exp_f32_e32 v31, v31
	v_pk_fma_f32 v[34:35], v[34:35], s[50:51], s[50:51] op_sel_hi:[1,0,0]
	v_pk_mul_f32 v[28:29], v[32:33], v[28:29]
	v_pk_mul_f32 v[32:33], v[24:25], s[44:45] op_sel_hi:[1,0]
	v_exp_f32_e32 v36, v36
	v_exp_f32_e32 v37, v37
	v_rcp_f32_e32 v34, v34
	v_rcp_f32_e32 v35, v35
	v_exp_f32_e32 v32, v32
	v_exp_f32_e32 v33, v33
	v_pk_fma_f32 v[30:31], v[30:31], s[50:51], s[50:51] op_sel_hi:[1,0,0]
	v_pk_fma_f32 v[36:37], v[36:37], s[50:51], s[50:51] op_sel_hi:[1,0,0]
	v_rcp_f32_e32 v30, v30
	v_rcp_f32_e32 v31, v31
	v_pk_mul_f32 v[26:27], v[34:35], v[26:27]
	v_pk_fma_f32 v[32:33], v[32:33], s[50:51], s[50:51] op_sel_hi:[1,0,0]
	v_pk_mul_f32 v[18:19], v[22:23], v[18:19]
	v_rcp_f32_e32 v36, v36
	v_rcp_f32_e32 v37, v37
	v_rcp_f32_e32 v32, v32
	v_rcp_f32_e32 v33, v33
	v_pk_mul_f32 v[20:21], v[24:25], v[20:21]
	v_pk_mul_f32 v[18:19], v[30:31], v[18:19]
	v_med3_f32 v23, v26, s80, v154
	v_med3_f32 v24, v27, s80, v154
	v_cvt_pk_fp8_f32 v22, v23, v24
	v_med3_f32 v18, v18, s80, v154
	v_med3_f32 v19, v19, s80, v154
	v_cvt_pk_fp8_f32 v23, v18, v19
	v_pk_mul_f32 v[28:29], v[36:37], v[28:29]
	v_pk_mul_f32 v[20:21], v[32:33], v[20:21]
	v_med3_f32 v24, v28, s80, v154
	v_med3_f32 v25, v29, s80, v154
	v_med3_f32 v18, v20, s80, v154
	v_med3_f32 v19, v21, s80, v154
	v_cvt_pk_fp8_f32 v22, v24, v25 op_sel:[0,0,1]
	v_cvt_pk_fp8_f32 v23, v18, v19 op_sel:[0,0,1]
	v_lshl_add_u64 v[250:251], v[250:251], 0, s[88:89]
	global_store_dwordx2 v[250:251], v[22:23], off
	v_pk_mul_f32 v[18:19], v[14:15], s[44:45] op_sel_hi:[1,0]
	v_pk_mul_f32 v[10:11], v[14:15], v[10:11]
	v_exp_f32_e32 v18, v18
	v_exp_f32_e32 v19, v19
	v_pk_mul_f32 v[14:15], v[6:7], s[44:45] op_sel_hi:[1,0]
	v_pk_mul_f32 v[20:21], v[16:17], s[44:45] op_sel_hi:[1,0]
	v_exp_f32_e32 v14, v14
	v_exp_f32_e32 v15, v15
	v_pk_fma_f32 v[18:19], v[18:19], s[50:51], s[50:51] op_sel_hi:[1,0,0]
	v_pk_mul_f32 v[12:13], v[16:17], v[12:13]
	v_pk_mul_f32 v[16:17], v[8:9], s[44:45] op_sel_hi:[1,0]
	v_exp_f32_e32 v20, v20
	v_exp_f32_e32 v21, v21
	v_rcp_f32_e32 v18, v18
	v_rcp_f32_e32 v19, v19
	v_exp_f32_e32 v16, v16
	v_exp_f32_e32 v17, v17
	v_pk_fma_f32 v[14:15], v[14:15], s[50:51], s[50:51] op_sel_hi:[1,0,0]
	v_pk_fma_f32 v[20:21], v[20:21], s[50:51], s[50:51] op_sel_hi:[1,0,0]
	v_rcp_f32_e32 v14, v14
	v_rcp_f32_e32 v15, v15
	v_pk_mul_f32 v[10:11], v[18:19], v[10:11]
	v_pk_fma_f32 v[16:17], v[16:17], s[50:51], s[50:51] op_sel_hi:[1,0,0]
	v_pk_mul_f32 v[2:3], v[6:7], v[2:3]
	v_rcp_f32_e32 v20, v20
	v_rcp_f32_e32 v21, v21
	v_rcp_f32_e32 v16, v16
	v_rcp_f32_e32 v17, v17
	v_pk_mul_f32 v[4:5], v[8:9], v[4:5]
	v_pk_mul_f32 v[2:3], v[14:15], v[2:3]
	v_med3_f32 v7, v10, s80, v154
	v_med3_f32 v8, v11, s80, v154
	v_cvt_pk_fp8_f32 v6, v7, v8
	v_med3_f32 v2, v2, s80, v154
	v_med3_f32 v3, v3, s80, v154
	v_cvt_pk_fp8_f32 v7, v2, v3
	v_pk_mul_f32 v[12:13], v[20:21], v[12:13]
	v_pk_mul_f32 v[4:5], v[16:17], v[4:5]
	v_med3_f32 v8, v12, s80, v154
	v_med3_f32 v9, v13, s80, v154
	v_med3_f32 v2, v4, s80, v154
	v_med3_f32 v3, v5, s80, v154
	v_cvt_pk_fp8_f32 v6, v8, v9 op_sel:[0,0,1]
	v_cvt_pk_fp8_f32 v7, v2, v3 op_sel:[0,0,1]
	s_andn2_b64 vcc, exec, s[0:1]
	s_mov_b64 s[0:1], -1
	v_lshl_add_u64 v[250:251], v[250:251], 0, s[88:89]
	global_store_dwordx2 v[250:251], v[6:7], off
	s_cbranch_vccnz .LBB0_779
	s_andn2_b64 vcc, exec, s[12:13]
	s_cbranch_vccnz .LBB0_778
	s_barrier
	s_branch .LBB0_778

.LBB0_1500:
	s_lshl_b32 s88, s71, 4
	s_mov_b32 s89, 0
	s_mul_i32 s90, s71, 0x50
	s_mov_b32 s91, 0
	v_pk_mul_f32 v[10:11], v[160:161], s[42:43] op_sel_hi:[1,0]
	v_pk_mul_f32 v[8:9], v[158:159], s[42:43] op_sel_hi:[1,0]
	v_exp_f32_e32 v10, v10
	v_exp_f32_e32 v11, v11
	v_exp_f32_e32 v8, v8
	v_exp_f32_e32 v9, v9
	v_pk_mul_f32 v[12:13], v[160:161], v[156:157]
	v_pk_fma_f32 v[10:11], v[10:11], s[44:45], s[44:45] op_sel_hi:[1,0,0]
	v_pk_mul_f32 v[14:15], v[158:159], v[154:155]
	v_rcp_f32_e32 v10, v10
	v_rcp_f32_e32 v11, v11
	v_pk_fma_f32 v[8:9], v[8:9], s[44:45], s[44:45] op_sel_hi:[1,0,0]
	v_pk_mul_f32 v[18:19], v[150:151], v[146:147]
	v_rcp_f32_e32 v8, v8
	v_rcp_f32_e32 v9, v9
	v_pk_mul_f32 v[10:11], v[12:13], v[10:11]
	v_pk_mul_f32 v[12:13], v[150:151], s[42:43] op_sel_hi:[1,0]
	v_pk_mul_f32 v[16:17], v[152:153], v[148:149]
	v_exp_f32_e32 v12, v12
	v_exp_f32_e32 v13, v13
	v_pk_mul_f32 v[8:9], v[14:15], v[8:9]
	v_pk_mul_f32 v[14:15], v[152:153], s[42:43] op_sel_hi:[1,0]
	v_med3_f32 v7, v8, s72, v191
	v_exp_f32_e32 v14, v14
	v_exp_f32_e32 v15, v15
	v_pk_fma_f32 v[12:13], v[12:13], s[44:45], s[44:45] op_sel_hi:[1,0,0]
	v_med3_f32 v9, v9, s72, v191
	v_rcp_f32_e32 v12, v12
	v_rcp_f32_e32 v13, v13
	v_pk_fma_f32 v[14:15], v[14:15], s[44:45], s[44:45] op_sel_hi:[1,0,0]
	v_rcp_f32_e32 v14, v14
	v_rcp_f32_e32 v15, v15
	v_pk_mul_f32 v[12:13], v[18:19], v[12:13]
	v_cvt_pk_fp8_f32 v8, v7, v9
	v_med3_f32 v7, v10, s72, v191
	v_med3_f32 v10, v11, s72, v191
	v_med3_f32 v11, v12, s72, v191
	v_med3_f32 v12, v13, s72, v191
	v_cvt_pk_fp8_f32 v9, v11, v12
	v_pk_mul_f32 v[14:15], v[16:17], v[14:15]
	v_readlane_b32 s4, v254, 56
	v_cvt_pk_fp8_f32 v8, v7, v10 op_sel:[0,0,1]
	v_med3_f32 v7, v14, s72, v191
	v_med3_f32 v10, v15, s72, v191
	v_readlane_b32 s5, v254, 57
	v_cvt_pk_fp8_f32 v9, v7, v10 op_sel:[0,0,1]
	v_lshl_add_u32 v6, s54, 8, v1
	v_lshl_or_b32 v2, s52, 7, v185
	v_mov_b64_e32 v[4:5], s[4:5]
	v_ashrrev_i32_e32 v3, 31, v2
	v_mad_i64_i32 v[10:11], s[4:5], v6, s71, v[4:5]
	v_lshl_add_u64 v[10:11], v[10:11], 0, v[2:3]
	s_nop 15
	s_nop 15
	global_store_dwordx2 v[10:11], v[8:9], off
	v_lshl_add_u64 v[250:251], v[10:11], 0, s[88:89]
	v_pk_mul_f32 v[8:9], v[142:143], s[42:43] op_sel_hi:[1,0]
	v_pk_mul_f32 v[10:11], v[144:145], s[42:43] op_sel_hi:[1,0]
	v_exp_f32_e32 v8, v8
	v_exp_f32_e32 v9, v9
	v_exp_f32_e32 v10, v10
	v_exp_f32_e32 v11, v11
	v_pk_mul_f32 v[12:13], v[144:145], v[140:141]
	v_pk_fma_f32 v[8:9], v[8:9], s[44:45], s[44:45] op_sel_hi:[1,0,0]
	v_pk_mul_f32 v[14:15], v[142:143], v[138:139]
	v_pk_fma_f32 v[10:11], v[10:11], s[44:45], s[44:45] op_sel_hi:[1,0,0]
	v_rcp_f32_e32 v8, v8
	v_rcp_f32_e32 v9, v9
	v_rcp_f32_e32 v10, v10
	v_rcp_f32_e32 v11, v11
	v_pk_mul_f32 v[16:17], v[136:137], v[132:133]
	v_pk_mul_f32 v[8:9], v[14:15], v[8:9]
	v_pk_mul_f32 v[14:15], v[136:137], s[42:43] op_sel_hi:[1,0]
	v_pk_mul_f32 v[10:11], v[12:13], v[10:11]
	v_pk_mul_f32 v[12:13], v[134:135], s[42:43] op_sel_hi:[1,0]
	v_exp_f32_e32 v14, v14
	v_exp_f32_e32 v12, v12
	v_exp_f32_e32 v13, v13
	v_exp_f32_e32 v15, v15
	v_pk_mul_f32 v[18:19], v[134:135], v[130:131]
	v_med3_f32 v9, v9, s72, v191
	v_pk_fma_f32 v[12:13], v[12:13], s[44:45], s[44:45] op_sel_hi:[1,0,0]
	v_pk_fma_f32 v[14:15], v[14:15], s[44:45], s[44:45] op_sel_hi:[1,0,0]
	v_rcp_f32_e32 v12, v12
	v_rcp_f32_e32 v13, v13
	v_rcp_f32_e32 v14, v14
	v_rcp_f32_e32 v15, v15
	v_med3_f32 v10, v10, s72, v191
	v_pk_mul_f32 v[12:13], v[18:19], v[12:13]
	v_med3_f32 v11, v11, s72, v191
	v_pk_mul_f32 v[14:15], v[16:17], v[14:15]
	v_med3_f32 v16, v8, s72, v191
	v_cvt_pk_fp8_f32 v8, v16, v9
	v_med3_f32 v12, v12, s72, v191
	v_med3_f32 v13, v13, s72, v191
	v_cvt_pk_fp8_f32 v9, v12, v13
	v_cvt_pk_fp8_f32 v8, v10, v11 op_sel:[0,0,1]
	v_med3_f32 v10, v14, s72, v191
	v_med3_f32 v11, v15, s72, v191
	v_cvt_pk_fp8_f32 v9, v10, v11 op_sel:[0,0,1]
	global_store_dwordx2 v[250:251], v[8:9], off
	v_pk_mul_f32 v[8:9], v[126:127], s[42:43] op_sel_hi:[1,0]
	v_pk_mul_f32 v[10:11], v[128:129], s[42:43] op_sel_hi:[1,0]
	v_exp_f32_e32 v8, v8
	v_exp_f32_e32 v9, v9
	v_exp_f32_e32 v10, v10
	v_exp_f32_e32 v11, v11
	v_pk_mul_f32 v[12:13], v[128:129], v[124:125]
	v_pk_fma_f32 v[8:9], v[8:9], s[44:45], s[44:45] op_sel_hi:[1,0,0]
	v_pk_mul_f32 v[14:15], v[126:127], v[122:123]
	v_pk_fma_f32 v[10:11], v[10:11], s[44:45], s[44:45] op_sel_hi:[1,0,0]
	v_rcp_f32_e32 v8, v8
	v_rcp_f32_e32 v9, v9
	v_rcp_f32_e32 v10, v10
	v_rcp_f32_e32 v11, v11
	v_pk_mul_f32 v[16:17], v[120:121], v[116:117]
	v_pk_mul_f32 v[8:9], v[14:15], v[8:9]
	v_pk_mul_f32 v[14:15], v[120:121], s[42:43] op_sel_hi:[1,0]
	v_pk_mul_f32 v[10:11], v[12:13], v[10:11]
	v_pk_mul_f32 v[12:13], v[118:119], s[42:43] op_sel_hi:[1,0]
	v_exp_f32_e32 v14, v14
	v_exp_f32_e32 v12, v12
	v_exp_f32_e32 v13, v13
	v_exp_f32_e32 v15, v15
	v_pk_mul_f32 v[18:19], v[118:119], v[114:115]
	v_med3_f32 v9, v9, s72, v191
	v_pk_fma_f32 v[12:13], v[12:13], s[44:45], s[44:45] op_sel_hi:[1,0,0]
	v_pk_fma_f32 v[14:15], v[14:15], s[44:45], s[44:45] op_sel_hi:[1,0,0]
	v_rcp_f32_e32 v12, v12
	v_rcp_f32_e32 v13, v13
	v_rcp_f32_e32 v14, v14
	v_rcp_f32_e32 v15, v15
	v_med3_f32 v10, v10, s72, v191
	v_pk_mul_f32 v[12:13], v[18:19], v[12:13]
	v_med3_f32 v11, v11, s72, v191
	v_pk_mul_f32 v[14:15], v[16:17], v[14:15]
	v_med3_f32 v16, v8, s72, v191
	v_cvt_pk_fp8_f32 v8, v16, v9
	v_med3_f32 v12, v12, s72, v191
	v_med3_f32 v13, v13, s72, v191
	v_cvt_pk_fp8_f32 v9, v12, v13
	v_cvt_pk_fp8_f32 v8, v10, v11 op_sel:[0,0,1]
	v_med3_f32 v10, v14, s72, v191
	v_med3_f32 v11, v15, s72, v191
	v_cvt_pk_fp8_f32 v9, v10, v11 op_sel:[0,0,1]
	v_lshl_add_u64 v[250:251], v[250:251], 0, s[88:89]
	global_store_dwordx2 v[250:251], v[8:9], off
	v_pk_mul_f32 v[8:9], v[110:111], s[42:43] op_sel_hi:[1,0]
	v_pk_mul_f32 v[10:11], v[112:113], s[42:43] op_sel_hi:[1,0]
	v_exp_f32_e32 v8, v8
	v_exp_f32_e32 v9, v9
	v_exp_f32_e32 v10, v10
	v_exp_f32_e32 v11, v11
	v_pk_mul_f32 v[12:13], v[112:113], v[108:109]
	v_pk_fma_f32 v[8:9], v[8:9], s[44:45], s[44:45] op_sel_hi:[1,0,0]
	v_pk_mul_f32 v[14:15], v[110:111], v[106:107]
	v_pk_fma_f32 v[10:11], v[10:11], s[44:45], s[44:45] op_sel_hi:[1,0,0]
	v_rcp_f32_e32 v8, v8
	v_rcp_f32_e32 v9, v9
	v_rcp_f32_e32 v10, v10
	v_rcp_f32_e32 v11, v11
	v_pk_mul_f32 v[16:17], v[104:105], v[100:101]
	v_pk_mul_f32 v[8:9], v[14:15], v[8:9]
	v_pk_mul_f32 v[14:15], v[104:105], s[42:43] op_sel_hi:[1,0]
	v_pk_mul_f32 v[10:11], v[12:13], v[10:11]
	v_pk_mul_f32 v[12:13], v[102:103], s[42:43] op_sel_hi:[1,0]
	v_exp_f32_e32 v14, v14
	v_exp_f32_e32 v12, v12
	v_exp_f32_e32 v13, v13
	v_exp_f32_e32 v15, v15
	v_pk_mul_f32 v[18:19], v[102:103], v[98:99]
	v_med3_f32 v9, v9, s72, v191
	v_pk_fma_f32 v[12:13], v[12:13], s[44:45], s[44:45] op_sel_hi:[1,0,0]
	v_pk_fma_f32 v[14:15], v[14:15], s[44:45], s[44:45] op_sel_hi:[1,0,0]
	v_rcp_f32_e32 v12, v12
	v_rcp_f32_e32 v13, v13
	v_rcp_f32_e32 v14, v14
	v_rcp_f32_e32 v15, v15
	v_med3_f32 v10, v10, s72, v191
	v_pk_mul_f32 v[12:13], v[18:19], v[12:13]
	v_med3_f32 v11, v11, s72, v191
	v_pk_mul_f32 v[14:15], v[16:17], v[14:15]
	v_med3_f32 v16, v8, s72, v191
	v_cvt_pk_fp8_f32 v8, v16, v9
	v_med3_f32 v12, v12, s72, v191
	v_med3_f32 v13, v13, s72, v191
	v_cvt_pk_fp8_f32 v9, v12, v13
	v_cvt_pk_fp8_f32 v8, v10, v11 op_sel:[0,0,1]
	v_med3_f32 v10, v14, s72, v191
	v_med3_f32 v11, v15, s72, v191
	v_cvt_pk_fp8_f32 v9, v10, v11 op_sel:[0,0,1]
	v_lshl_add_u64 v[250:251], v[250:251], 0, s[88:89]
	global_store_dwordx2 v[250:251], v[8:9], off
	v_pk_mul_f32 v[8:9], v[94:95], s[42:43] op_sel_hi:[1,0]
	v_pk_mul_f32 v[10:11], v[96:97], s[42:43] op_sel_hi:[1,0]
	v_exp_f32_e32 v8, v8
	v_exp_f32_e32 v9, v9
	v_exp_f32_e32 v10, v10
	v_exp_f32_e32 v11, v11
	v_pk_mul_f32 v[12:13], v[96:97], v[92:93]
	v_pk_fma_f32 v[8:9], v[8:9], s[44:45], s[44:45] op_sel_hi:[1,0,0]
	v_pk_mul_f32 v[14:15], v[94:95], v[90:91]
	v_pk_fma_f32 v[10:11], v[10:11], s[44:45], s[44:45] op_sel_hi:[1,0,0]
	v_rcp_f32_e32 v8, v8
	v_rcp_f32_e32 v9, v9
	v_rcp_f32_e32 v10, v10
	v_rcp_f32_e32 v11, v11
	v_pk_mul_f32 v[16:17], v[88:89], v[84:85]
	v_pk_mul_f32 v[8:9], v[14:15], v[8:9]
	v_pk_mul_f32 v[14:15], v[88:89], s[42:43] op_sel_hi:[1,0]
	v_pk_mul_f32 v[10:11], v[12:13], v[10:11]
	v_pk_mul_f32 v[12:13], v[86:87], s[42:43] op_sel_hi:[1,0]
	v_exp_f32_e32 v14, v14
	v_exp_f32_e32 v12, v12
	v_exp_f32_e32 v13, v13
	v_exp_f32_e32 v15, v15
	v_pk_mul_f32 v[18:19], v[86:87], v[82:83]
	v_med3_f32 v9, v9, s72, v191
	v_pk_fma_f32 v[12:13], v[12:13], s[44:45], s[44:45] op_sel_hi:[1,0,0]
	v_pk_fma_f32 v[14:15], v[14:15], s[44:45], s[44:45] op_sel_hi:[1,0,0]
	v_rcp_f32_e32 v12, v12
	v_rcp_f32_e32 v13, v13
	v_rcp_f32_e32 v14, v14
	v_rcp_f32_e32 v15, v15
	v_med3_f32 v10, v10, s72, v191
	v_pk_mul_f32 v[12:13], v[18:19], v[12:13]
	v_med3_f32 v11, v11, s72, v191
	v_pk_mul_f32 v[14:15], v[16:17], v[14:15]
	v_med3_f32 v16, v8, s72, v191
	v_cvt_pk_fp8_f32 v8, v16, v9
	v_med3_f32 v12, v12, s72, v191
	v_med3_f32 v13, v13, s72, v191
	v_cvt_pk_fp8_f32 v9, v12, v13
	v_cvt_pk_fp8_f32 v8, v10, v11 op_sel:[0,0,1]
	v_med3_f32 v10, v14, s72, v191
	v_med3_f32 v11, v15, s72, v191
	v_cvt_pk_fp8_f32 v9, v10, v11 op_sel:[0,0,1]
	v_lshl_add_u64 v[250:251], v[250:251], 0, s[90:91]
	global_store_dwordx2 v[250:251], v[8:9], off
	v_pk_mul_f32 v[8:9], v[78:79], s[42:43] op_sel_hi:[1,0]
	v_pk_mul_f32 v[10:11], v[80:81], s[42:43] op_sel_hi:[1,0]
	v_exp_f32_e32 v8, v8
	v_exp_f32_e32 v9, v9
	v_exp_f32_e32 v10, v10
	v_exp_f32_e32 v11, v11
	v_pk_mul_f32 v[12:13], v[80:81], v[76:77]
	v_pk_fma_f32 v[8:9], v[8:9], s[44:45], s[44:45] op_sel_hi:[1,0,0]
	v_pk_mul_f32 v[14:15], v[78:79], v[74:75]
	v_pk_fma_f32 v[10:11], v[10:11], s[44:45], s[44:45] op_sel_hi:[1,0,0]
	v_rcp_f32_e32 v8, v8
	v_rcp_f32_e32 v9, v9
	v_rcp_f32_e32 v10, v10
	v_rcp_f32_e32 v11, v11
	v_pk_mul_f32 v[16:17], v[72:73], v[68:69]
	v_pk_mul_f32 v[8:9], v[14:15], v[8:9]
	v_pk_mul_f32 v[14:15], v[72:73], s[42:43] op_sel_hi:[1,0]
	v_pk_mul_f32 v[10:11], v[12:13], v[10:11]
	v_pk_mul_f32 v[12:13], v[70:71], s[42:43] op_sel_hi:[1,0]
	v_exp_f32_e32 v14, v14
	v_exp_f32_e32 v12, v12
	v_exp_f32_e32 v13, v13
	v_exp_f32_e32 v15, v15
	v_pk_mul_f32 v[18:19], v[70:71], v[66:67]
	v_med3_f32 v9, v9, s72, v191
	v_pk_fma_f32 v[12:13], v[12:13], s[44:45], s[44:45] op_sel_hi:[1,0,0]
	v_pk_fma_f32 v[14:15], v[14:15], s[44:45], s[44:45] op_sel_hi:[1,0,0]
	v_rcp_f32_e32 v12, v12
	v_rcp_f32_e32 v13, v13
	v_rcp_f32_e32 v14, v14
	v_rcp_f32_e32 v15, v15
	v_med3_f32 v10, v10, s72, v191
	v_pk_mul_f32 v[12:13], v[18:19], v[12:13]
	v_med3_f32 v11, v11, s72, v191
	v_pk_mul_f32 v[14:15], v[16:17], v[14:15]
	v_med3_f32 v16, v8, s72, v191
	v_cvt_pk_fp8_f32 v8, v16, v9
	v_med3_f32 v12, v12, s72, v191
	v_med3_f32 v13, v13, s72, v191
	v_cvt_pk_fp8_f32 v9, v12, v13
	v_cvt_pk_fp8_f32 v8, v10, v11 op_sel:[0,0,1]
	v_med3_f32 v10, v14, s72, v191
	v_med3_f32 v11, v15, s72, v191
	v_cvt_pk_fp8_f32 v9, v10, v11 op_sel:[0,0,1]
	v_lshl_add_u64 v[250:251], v[250:251], 0, s[88:89]
	global_store_dwordx2 v[250:251], v[8:9], off
	v_pk_mul_f32 v[8:9], v[62:63], s[42:43] op_sel_hi:[1,0]
	v_pk_mul_f32 v[10:11], v[64:65], s[42:43] op_sel_hi:[1,0]
	v_exp_f32_e32 v8, v8
	v_exp_f32_e32 v9, v9
	v_exp_f32_e32 v10, v10
	v_exp_f32_e32 v11, v11
	v_pk_mul_f32 v[12:13], v[64:65], v[60:61]
	v_pk_fma_f32 v[8:9], v[8:9], s[44:45], s[44:45] op_sel_hi:[1,0,0]
	v_pk_mul_f32 v[14:15], v[62:63], v[58:59]
	v_pk_fma_f32 v[10:11], v[10:11], s[44:45], s[44:45] op_sel_hi:[1,0,0]
	v_rcp_f32_e32 v8, v8
	v_rcp_f32_e32 v9, v9
	v_rcp_f32_e32 v10, v10
	v_rcp_f32_e32 v11, v11
	v_pk_mul_f32 v[16:17], v[56:57], v[52:53]
	v_pk_mul_f32 v[8:9], v[14:15], v[8:9]
	v_pk_mul_f32 v[14:15], v[56:57], s[42:43] op_sel_hi:[1,0]
	v_pk_mul_f32 v[10:11], v[12:13], v[10:11]
	v_pk_mul_f32 v[12:13], v[54:55], s[42:43] op_sel_hi:[1,0]
	v_exp_f32_e32 v14, v14
	v_exp_f32_e32 v12, v12
	v_exp_f32_e32 v13, v13
	v_exp_f32_e32 v15, v15
	v_pk_mul_f32 v[18:19], v[54:55], v[50:51]
	v_med3_f32 v9, v9, s72, v191
	v_pk_fma_f32 v[12:13], v[12:13], s[44:45], s[44:45] op_sel_hi:[1,0,0]
	v_pk_fma_f32 v[14:15], v[14:15], s[44:45], s[44:45] op_sel_hi:[1,0,0]
	v_rcp_f32_e32 v12, v12
	v_rcp_f32_e32 v13, v13
	v_rcp_f32_e32 v14, v14
	v_rcp_f32_e32 v15, v15
	v_med3_f32 v10, v10, s72, v191
	v_pk_mul_f32 v[12:13], v[18:19], v[12:13]
	v_med3_f32 v11, v11, s72, v191
	v_pk_mul_f32 v[14:15], v[16:17], v[14:15]
	v_med3_f32 v16, v8, s72, v191
	v_cvt_pk_fp8_f32 v8, v16, v9
	v_med3_f32 v12, v12, s72, v191
	v_med3_f32 v13, v13, s72, v191
	v_cvt_pk_fp8_f32 v9, v12, v13
	v_cvt_pk_fp8_f32 v8, v10, v11 op_sel:[0,0,1]
	v_med3_f32 v10, v14, s72, v191
	v_med3_f32 v11, v15, s72, v191
	v_cvt_pk_fp8_f32 v9, v10, v11 op_sel:[0,0,1]
	v_lshl_add_u64 v[250:251], v[250:251], 0, s[88:89]
	global_store_dwordx2 v[250:251], v[8:9], off
	v_pk_mul_f32 v[6:7], v[46:47], s[42:43] op_sel_hi:[1,0]
	v_pk_mul_f32 v[8:9], v[48:49], s[42:43] op_sel_hi:[1,0]
	v_exp_f32_e32 v6, v6
	v_exp_f32_e32 v7, v7
	v_exp_f32_e32 v8, v8
	v_exp_f32_e32 v9, v9
	v_pk_mul_f32 v[10:11], v[48:49], v[44:45]
	v_pk_fma_f32 v[6:7], v[6:7], s[44:45], s[44:45] op_sel_hi:[1,0,0]
	v_pk_mul_f32 v[12:13], v[46:47], v[42:43]
	v_pk_fma_f32 v[8:9], v[8:9], s[44:45], s[44:45] op_sel_hi:[1,0,0]
	v_rcp_f32_e32 v6, v6
	v_rcp_f32_e32 v7, v7
	v_rcp_f32_e32 v8, v8
	v_rcp_f32_e32 v9, v9
	v_pk_mul_f32 v[14:15], v[40:41], v[36:37]
	v_pk_mul_f32 v[6:7], v[12:13], v[6:7]
	v_pk_mul_f32 v[12:13], v[40:41], s[42:43] op_sel_hi:[1,0]
	v_pk_mul_f32 v[8:9], v[10:11], v[8:9]
	v_pk_mul_f32 v[10:11], v[38:39], s[42:43] op_sel_hi:[1,0]
	v_exp_f32_e32 v12, v12
	v_exp_f32_e32 v10, v10
	v_exp_f32_e32 v11, v11
	v_exp_f32_e32 v13, v13
	v_pk_mul_f32 v[16:17], v[38:39], v[34:35]
	v_med3_f32 v7, v7, s72, v191
	v_pk_fma_f32 v[10:11], v[10:11], s[44:45], s[44:45] op_sel_hi:[1,0,0]
	v_pk_fma_f32 v[12:13], v[12:13], s[44:45], s[44:45] op_sel_hi:[1,0,0]
	v_rcp_f32_e32 v10, v10
	v_rcp_f32_e32 v11, v11
	v_rcp_f32_e32 v12, v12
	v_rcp_f32_e32 v13, v13
	v_med3_f32 v8, v8, s72, v191
	v_pk_mul_f32 v[10:11], v[16:17], v[10:11]
	v_med3_f32 v9, v9, s72, v191
	v_pk_mul_f32 v[12:13], v[14:15], v[12:13]
	v_med3_f32 v14, v6, s72, v191
	v_cvt_pk_fp8_f32 v6, v14, v7
	v_med3_f32 v10, v10, s72, v191
	v_med3_f32 v11, v11, s72, v191
	v_cvt_pk_fp8_f32 v7, v10, v11
	v_cvt_pk_fp8_f32 v6, v8, v9 op_sel:[0,0,1]
	v_med3_f32 v8, v12, s72, v191
	v_med3_f32 v9, v13, s72, v191
	v_cvt_pk_fp8_f32 v7, v8, v9 op_sel:[0,0,1]
	s_and_b64 vcc, exec, s[0:1]
	s_mov_b64 s[0:1], -1
	v_lshl_add_u64 v[250:251], v[250:251], 0, s[88:89]
	global_store_dwordx2 v[250:251], v[6:7], off
	s_cbranch_vccnz .LBB0_1487
	s_andn2_b64 vcc, exec, s[18:19]
	s_cbranch_vccnz .LBB0_1486
	s_barrier
	s_branch .LBB0_1486
